# merge-phase non-temporal loads switched to the default cache policy
# speedup vs baseline: 1.0079x; 1.0079x over previous
; __device__ __forceinline__ void merge_phase(const bf16_t* atto, const float* lse, const bf16_t* ob, const float* ssq, const bf16_t* proj, const float* gla_gain, bf16_t* ya, bf16_t* yb,
;                                             int vcu, int G, int wave, int lane) {
;     ...
;     for (int row0 = 2 * gw; row0 < T; row0 += 2 * NGW) {
;         float l0[2], l1[2], l2[2]; u32x4 a0[2], a1[2], a2[2], o[2][2], rr_[2][2]; f32x4 sq[2][2][4];
; #pragma unroll
;         for (int r = 0; r < 2; ++r) { const int row = row0 + r;
;             l0[r] = lse[((size_t)0 * T + row) * 4 + hj]; l1[r] = lse[((size_t)1 * T + row) * 4 + hj]; l2[r] = lse[((size_t)2 * T + row) * 4 + hj];
;             a0[r] = __builtin_nontemporal_load((const u32x4*)(atto + ((size_t)0 * T + row) * 512 + 8 * lane)); a1[r] = __builtin_nontemporal_load((const u32x4*)(atto + ((size_t)1 * T + row) * 512 + 8 * lane)); a2[r] = __builtin_nontemporal_load((const u32x4*)(atto + ((size_t)2 * T + row) * 512 + 8 * lane));
; #pragma unroll
;             for (int c = 0; c < 2; ++c) { const int col = 8 * lane + 512 * c, hh = col >> 8;
;                 const f32x4* sp = (const f32x4*)(ssq + ((size_t)row * 4 + hh) * 16); sq[r][c][0] = sp[0]; sq[r][c][1] = sp[1]; sq[r][c][2] = sp[2]; sq[r][c][3] = sp[3];
;                 o[r][c] = __builtin_nontemporal_load((const u32x4*)(ob + (size_t)row * 1024 + col));
;     ...
;                 { const u32x2 r8 = *(const u32x2*)((const unsigned char*)proj + (size_t)row * NP * 2 + G8_BYTE0 + col); rr_[r][c] = (u32x4){r8.x, r8.y, 0u, 0u}; }
;     ...
;                 rr_[r][c] = *(const u32x4*)(proj + (size_t)row * NP + RB + col);
;     ...
;             } }
; #pragma unroll
;         for (int r = 0; r < 2; ++r) { const int row = row0 + r;
;             const float m = fmaxf(l0[r], fmaxf(l1[r], l2[r])); float e0 = __expf(l0[r] - m), e1 = __expf(l1[r] - m), e2 = __expf(l2[r] - m); const float inv = 1.0f / (e0 + e1 + e2); e0 *= inv; e1 *= inv; e2 *= inv;
.LBB0_484:
	s_waitcnt lgkmcnt(0)
	v_lshl_add_u64 v[16:17], s[6:7], 0, v[130:131]
	v_add_co_u32_e32 v18, vcc, 0x400000, v16
	v_lshl_add_u64 v[22:23], s[6:7], 0, v[128:129]
	s_nop 0
	v_addc_co_u32_e32 v19, vcc, 0, v17, vcc
	v_add_co_u32_e32 v20, vcc, 0x440000, v16
	global_load_dword v152, v[18:19], off
	s_nop 0
	v_addc_co_u32_e32 v21, vcc, 0, v17, vcc
	v_add_co_u32_e32 v16, vcc, 0x480000, v16
	global_load_dword v153, v[20:21], off
	s_nop 0
	v_addc_co_u32_e32 v17, vcc, 0, v17, vcc
	v_add_co_u32_e32 v24, vcc, 0x2b600000, v22
	v_lshl_add_u64 v[28:29], s[6:7], 0, v[134:135]
	s_nop 0
	v_addc_co_u32_e32 v25, vcc, 0, v23, vcc
	v_add_co_u32_e32 v26, vcc, 0x2c600000, v22
	global_load_dwordx4 v[110:113], v[24:25], off
	s_nop 0
	v_addc_co_u32_e32 v27, vcc, 0, v23, vcc
	v_add_co_u32_e32 v22, vcc, 0x2d600000, v22
	global_load_dwordx4 v[114:117], v[26:27], off
	s_nop 0
	v_addc_co_u32_e32 v23, vcc, 0, v23, vcc
	global_load_dwordx4 v[118:121], v[22:23], off
	global_load_dword v154, v[16:17], off
	v_add_co_u32_e32 v34, vcc, 0x500000, v28
	v_lshl_add_u64 v[30:31], v[28:29], 0, s[22:23]
	s_nop 0
	v_addc_co_u32_e32 v35, vcc, 0, v29, vcc
	global_load_dwordx4 v[106:109], v[34:35], off
	global_load_dwordx4 v[94:97], v[30:31], off offset:48
	global_load_dwordx4 v[98:101], v[30:31], off offset:32
	global_load_dwordx4 v[102:105], v[30:31], off offset:16
	v_lshl_add_u64 v[30:31], s[6:7], 0, v[126:127]
	s_mov_b32 s1, 0x2e600000
	v_add_co_u32_e32 v136, vcc, s1, v30
	s_mov_b32 s1, 0x30603000
	s_nop 0
	v_addc_co_u32_e32 v137, vcc, 0, v31, vcc
	v_lshl_add_u64 v[30:31], s[6:7], 0, v[124:125]
	v_add_co_u32_e32 v36, vcc, s1, v30
	v_lshl_add_u64 v[146:147], s[6:7], 0, v[132:133]
	s_nop 0
	v_addc_co_u32_e32 v37, vcc, 0, v31, vcc
	s_mov_b32 s1, 0x500000
	v_add_co_u32_e32 v148, vcc, s1, v146
	s_mov_b32 s1, 0x30609000
	s_nop 0
	v_addc_co_u32_e32 v149, vcc, 0, v147, vcc
	global_load_dwordx4 v[90:93], v[136:137], off
	global_load_dwordx2 v[142:143], v[36:37], off offset:1024
	v_lshl_add_u64 v[38:39], v[146:147], 0, s[22:23]
	global_load_dwordx4 v[86:89], v[148:149], off
	global_load_dwordx4 v[74:77], v[38:39], off offset:48
	global_load_dwordx4 v[78:81], v[38:39], off offset:32
	global_load_dwordx4 v[82:85], v[38:39], off offset:16
	global_load_dwordx4 v[70:73], v[136:137], off offset:1024
	global_load_dwordx2 v[140:141], v[36:37], off offset:1536
	global_load_dword v145, v[18:19], off offset:16
	global_load_dword v144, v[20:21], off offset:16
	global_load_dword v32, v[16:17], off offset:16
	global_load_dwordx4 v[62:65], v[24:25], off offset:1024
	global_load_dwordx4 v[66:69], v[26:27], off offset:1024
	global_load_dwordx4 v[58:61], v[22:23], off offset:1024
	v_lshl_add_u64 v[16:17], v[28:29], 0, s[24:25]
	v_add_co_u32_e32 v150, vcc, s1, v30
	global_load_dwordx4 v[54:57], v[34:35], off offset:256
	global_load_dwordx4 v[42:45], v[16:17], off offset:48
	global_load_dwordx4 v[46:49], v[16:17], off offset:32
	global_load_dwordx4 v[50:53], v[16:17], off offset:16
	global_load_dwordx4 v[38:41], v[136:137], off offset:2048
	v_addc_co_u32_e32 v151, vcc, 0, v31, vcc
	v_lshl_add_u64 v[16:17], v[146:147], 0, s[24:25]
	global_load_dwordx2 v[138:139], v[150:151], off offset:512
	global_load_dwordx4 v[34:37], v[148:149], off offset:256
	global_load_dwordx4 v[20:23], v[16:17], off offset:48
	global_load_dwordx4 v[24:27], v[16:17], off offset:32
	global_load_dwordx4 v[28:31], v[16:17], off offset:16
	s_nop 0
	global_load_dwordx4 v[16:19], v[136:137], off offset:3072
	s_nop 0
	global_load_dwordx2 v[136:137], v[150:151], off offset:1024
	s_mov_b32 s1, 0x24600000
	s_add_i32 s0, s0, s8
	v_lshl_add_u64 v[124:125], v[124:125], 0, s[12:13]
	v_lshl_add_u64 v[126:127], v[126:127], 0, s[14:15]
	v_lshl_add_u64 v[128:129], v[128:129], 0, s[16:17]
	v_lshl_add_u64 v[130:131], v[130:131], 0, s[18:19]
	v_lshl_add_u64 v[132:133], v[132:133], 0, s[20:21]
	v_lshl_add_u64 v[134:135], v[134:135], 0, s[20:21]
	s_cmpk_lt_i32 s0, 0x4000
	s_waitcnt vmcnt(31)
	v_and_b32_e32 v155, 0xffff0000, v118
	s_waitcnt vmcnt(30)
	v_max3_f32 v148, v152, v153, v154
	v_sub_f32_e32 v146, v152, v148
	v_mul_f32_e32 v146, 0x3fb8aa3b, v146
	v_exp_f32_e32 v147, v146
	v_sub_f32_e32 v146, v153, v148
	v_mul_f32_e32 v146, 0x3fb8aa3b, v146
	v_sub_f32_e32 v148, v154, v148
	v_exp_f32_e32 v146, v146
	v_mul_f32_e32 v148, 0x3fb8aa3b, v148
	v_exp_f32_e32 v149, v148
	s_waitcnt vmcnt(27)
; __device__ __forceinline__ unsigned pk2(float lo, float hi) { const f32x2_t v = {lo, hi}; const bf16x2_t b = __builtin_convertvector(v, bf16x2_t); return __builtin_bit_cast(unsigned, b); }
; __device__ __forceinline__ unsigned pk_fp8x4(float a, float b, float c, float d) { int p = __builtin_amdgcn_cvt_pk_fp8_f32(sat8(a), sat8(b), 0, false); p = __builtin_amdgcn_cvt_pk_fp8_f32(sat8(c), sat8(d), p, true); return (unsigned)p; }
; __device__ __forceinline__ void merge_phase(const bf16_t* atto, const float* lse, const bf16_t* ob, const float* ssq, const bf16_t* proj, const float* gla_gain, bf16_t* ya, bf16_t* yb,
;                                             int vcu, int G, int wave, int lane) {
;     ...
;         for (int r = 0; r < 2; ++r) { const int row = row0 + r;
;             const float m = fmaxf(l0[r], fmaxf(l1[r], l2[r])); float e0 = __expf(l0[r] - m), e1 = __expf(l1[r] - m), e2 = __expf(l2[r] - m); const float inv = 1.0f / (e0 + e1 + e2); e0 *= inv; e1 *= inv; e2 *= inv;
;             u32x4 w;
;             w.x = pk2(e0 * bflo(a0[r].x) + e1 * bflo(a1[r].x) + e2 * bflo(a2[r].x), e0 * bfhi(a0[r].x) + e1 * bfhi(a1[r].x) + e2 * bfhi(a2[r].x));
;             w.y = pk2(e0 * bflo(a0[r].y) + e1 * bflo(a1[r].y) + e2 * bflo(a2[r].y), e0 * bfhi(a0[r].y) + e1 * bfhi(a1[r].y) + e2 * bfhi(a2[r].y));
;             w.z = pk2(e0 * bflo(a0[r].z) + e1 * bflo(a1[r].z) + e2 * bflo(a2[r].z), e0 * bfhi(a0[r].z) + e1 * bfhi(a1[r].z) + e2 * bfhi(a2[r].z));
;             w.w = pk2(e0 * bflo(a0[r].w) + e1 * bflo(a1[r].w) + e2 * bflo(a2[r].w), e0 * bfhi(a0[r].w) + e1 * bfhi(a1[r].w) + e2 * bfhi(a2[r].w));
;     ...
;             { u32x2 w8; w8.x = pk_fp8x4(bflo(w.x), bfhi(w.x), bflo(w.y), bfhi(w.y)); w8.y = pk_fp8x4(bflo(w.z), bfhi(w.z), bflo(w.w), bfhi(w.w)); *(u32x2*)((unsigned char*)ya + (BR_FUSE ? (size_t)row * 1536 + 1024 : (size_t)row * 512) + 8 * lane) = w8; }
;     ...
;             *(u32x4*)(ya + (size_t)row * 512 + 8 * lane) = w;
;     ...
; #pragma unroll
;             for (int c = 0; c < 2; ++c) { const int col = 8 * lane + 512 * c;
;                 const f32x4 s0 = sq[r][c][0], s1 = sq[r][c][1], s2 = sq[r][c][2], s3 = sq[r][c][3];
;                 const float tot = ((s0[0] + s0[1]) + (s0[2] + s0[3])) + ((s1[0] + s1[1]) + (s1[2] + s1[3])) + ((s2[0] + s2[1]) + (s2[2] + s2[3])) + ((s3[0] + s3[1]) + (s3[2] + s3[3]));
;                 const float rstd = 1.0f / sqrtf(tot * (1.0f / 256.0f) + NORM_EPS);
	v_add_f32_e32 v98, v98, v99
	v_add_f32_e32 v148, v147, v146
	v_add_f32_e32 v100, v100, v101
	v_add_f32_e32 v148, v149, v148
	v_div_scale_f32 v150, s[2:3], v148, v148, 1.0
	v_rcp_f32_e32 v151, v150
	v_mov_b32_e32 v99, v96
	v_mov_b32_e32 v101, v97
	v_pk_add_f32 v[96:97], v[98:99], v[100:101]
	v_fma_f32 v152, -v150, v151, 1.0
	v_fmac_f32_e32 v151, v152, v151
	v_div_scale_f32 v152, vcc, 1.0, v148, 1.0
	v_mul_f32_e32 v153, v152, v151
	v_fma_f32 v154, -v150, v153, v152
	v_fmac_f32_e32 v153, v154, v151
	v_fma_f32 v150, -v150, v153, v152
	v_div_fmas_f32 v150, v150, v151, v153
	v_div_fixup_f32 v148, v150, v148, 1.0
	v_pk_mul_f32 v[146:147], v[146:147], v[148:149] op_sel_hi:[1,0]
	v_lshlrev_b32_e32 v152, 16, v110
	v_and_b32_e32 v153, 0xffff0000, v114
	v_mul_f32_e32 v150, v149, v148
	v_lshlrev_b32_e32 v148, 16, v114
	v_and_b32_e32 v149, 0xffff0000, v110
	v_pk_mul_f32 v[152:153], v[146:147], v[152:153] op_sel:[1,0] op_sel_hi:[0,1]
	v_lshlrev_b32_e32 v154, 16, v118
	v_pk_fma_f32 v[148:149], v[146:147], v[148:149], v[152:153]
	v_lshlrev_b32_e32 v110, 16, v111
	v_pk_fma_f32 v[148:149], v[150:151], v[154:155], v[148:149] op_sel_hi:[0,1,1]
	v_cvt_pk_bf16_f32 v151, v148, v149
	v_and_b32_e32 v149, 0xffff0000, v111
	v_and_b32_e32 v111, 0xffff0000, v115
	v_lshlrev_b32_e32 v148, 16, v115
	v_pk_mul_f32 v[110:111], v[146:147], v[110:111] op_sel:[1,0] op_sel_hi:[0,1]
	v_lshlrev_b32_e32 v114, 16, v119
	v_and_b32_e32 v115, 0xffff0000, v119
	v_pk_fma_f32 v[110:111], v[146:147], v[148:149], v[110:111]
	v_lshlrev_b32_e32 v118, 16, v120
	v_pk_fma_f32 v[110:111], v[150:151], v[114:115], v[110:111] op_sel_hi:[0,1,1]
	v_lshlrev_b32_e32 v114, 16, v112
	v_and_b32_e32 v115, 0xffff0000, v116
	v_cvt_pk_bf16_f32 v148, v110, v111
	v_lshlrev_b32_e32 v110, 16, v116
	v_and_b32_e32 v111, 0xffff0000, v112
	v_pk_mul_f32 v[114:115], v[146:147], v[114:115] op_sel:[1,0] op_sel_hi:[0,1]
	v_and_b32_e32 v119, 0xffff0000, v120
	v_pk_fma_f32 v[110:111], v[146:147], v[110:111], v[114:115]
	v_lshlrev_b32_e32 v112, 16, v113
	v_pk_fma_f32 v[110:111], v[150:151], v[118:119], v[110:111] op_sel_hi:[0,1,1]
	v_cvt_pk_bf16_f32 v114, v110, v111
	v_and_b32_e32 v111, 0xffff0000, v113
	v_and_b32_e32 v113, 0xffff0000, v117
	v_lshlrev_b32_e32 v110, 16, v117
	v_pk_mul_f32 v[112:113], v[146:147], v[112:113] op_sel:[1,0] op_sel_hi:[0,1]
	v_pk_fma_f32 v[110:111], v[146:147], v[110:111], v[112:113]
	v_lshlrev_b32_e32 v112, 16, v121
	v_and_b32_e32 v113, 0xffff0000, v121
	v_pk_fma_f32 v[110:111], v[150:151], v[112:113], v[110:111] op_sel_hi:[0,1,1]
	v_cvt_pk_bf16_f32 v110, v110, v111
	v_lshlrev_b32_e32 v111, 16, v151
	v_and_b32_e32 v112, 0xffff0000, v151
	v_med3_f32 v111, v111, s70, v190
	v_med3_f32 v116, v112, s70, v190
	v_mov_b32_e32 v112, v33
	v_cvt_pk_fp8_f32 v112, v111, v116
	v_lshlrev_b32_e32 v113, 16, v148
	v_and_b32_e32 v115, 0xffff0000, v148
	v_med3_f32 v111, v113, s70, v190
	v_med3_f32 v113, v115, s70, v190
	v_cvt_pk_fp8_f32 v112, v111, v113 op_sel:[0,0,1]
	v_lshlrev_b32_e32 v111, 16, v114
	v_and_b32_e32 v113, 0xffff0000, v114
	v_med3_f32 v111, v111, s70, v190
	v_med3_f32 v115, v113, s70, v190
	v_mov_b32_e32 v113, v33
	v_cvt_pk_fp8_f32 v113, v111, v115
	v_lshlrev_b32_e32 v114, 16, v110
	v_and_b32_e32 v110, 0xffff0000, v110
	v_med3_f32 v111, v114, s70, v190
	v_med3_f32 v110, v110, s70, v190
	v_cvt_pk_fp8_f32 v113, v111, v110 op_sel:[0,0,1]
	v_lshl_add_u64 v[110:111], s[6:7], 0, v[122:123]
	v_add_co_u32_e32 v110, vcc, s1, v110
	s_waitcnt vmcnt(24)
	v_cvt_pk_f32_fp8_e32 v[100:101], v143
	v_addc_co_u32_e32 v111, vcc, 0, v111, vcc
	global_store_dwordx2 v[110:111], v[112:113], off offset:1024
	v_mov_b32_e32 v112, v107
	v_mov_b32_e32 v113, v108
	v_mov_b32_e32 v107, v109
	v_mov_b32_e32 v108, v103
	v_mov_b32_e32 v109, v104
	v_mov_b32_e32 v103, v105
	v_pk_add_f32 v[106:107], v[112:113], v[106:107]
	v_pk_add_f32 v[102:103], v[108:109], v[102:103]
	v_pk_add_f32 v[106:107], v[106:107], v[106:107] op_sel:[0,1] op_sel_hi:[1,0]
	v_pk_add_f32 v[102:103], v[102:103], v[102:103] op_sel:[0,1] op_sel_hi:[1,0]
	v_mov_b32_e32 v107, v94
	v_mov_b32_e32 v103, v95
	v_pk_add_f32 v[94:95], v[106:107], v[102:103]
	v_lshlrev_b32_e32 v106, 16, v90
	v_pk_add_f32 v[94:95], v[94:95], v[96:97]
	v_and_b32_e32 v107, 0xffff0000, v90
	v_add_f32_e32 v94, v94, v95
	v_fmamk_f32 v94, v94, 0x3b800000, v183
	v_cmp_gt_f32_e32 vcc, s83, v94
	v_mul_f32_e32 v95, 0x4f800000, v94
	v_cvt_pk_f32_fp8_sdwa v[102:103], v143 src0_sel:WORD_1
	v_cndmask_b32_e32 v94, v94, v95, vcc
	v_sqrt_f32_e32 v95, v94
	s_waitcnt vmcnt(22)
	v_add_f32_e32 v78, v78, v79
	v_add_f32_e32 v80, v80, v81
	v_mov_b32_e32 v79, v76
	v_add_u32_e32 v96, -1, v95
	v_fma_f32 v97, -v96, v95, v94
	v_cmp_ge_f32_e64 s[4:5], 0, v97
	v_add_u32_e32 v97, 1, v95
	v_mov_b32_e32 v81, v77
	v_cndmask_b32_e64 v96, v95, v96, s[4:5]
	v_fma_f32 v95, -v97, v95, v94
	v_cmp_lt_f32_e64 s[4:5], 0, v95
	v_pk_add_f32 v[76:77], v[78:79], v[80:81]
	s_waitcnt vmcnt(19)
	v_cvt_pk_f32_fp8_e32 v[80:81], v141
	v_cndmask_b32_e64 v95, v96, v97, s[4:5]
	v_mul_f32_e32 v96, 0x37800000, v95
	v_cndmask_b32_e32 v95, v95, v96, vcc
	v_cmp_class_f32_e32 vcc, v94, v184
	s_waitcnt vmcnt(10)
	v_add_f32_e32 v46, v46, v47
	v_add_f32_e32 v48, v48, v49
	v_cndmask_b32_e32 v94, v95, v94, vcc
	v_div_scale_f32 v95, s[2:3], v94, v94, 1.0
	v_rcp_f32_e32 v96, v95
	v_mov_b32_e32 v47, v44
	v_mov_b32_e32 v49, v45
	v_pk_add_f32 v[44:45], v[46:47], v[48:49]
	v_fma_f32 v97, -v95, v96, 1.0
	v_fmac_f32_e32 v96, v97, v96
	v_div_scale_f32 v97, vcc, 1.0, v94, 1.0
	v_mul_f32_e32 v98, v97, v96
	v_fma_f32 v99, -v95, v98, v97
	v_fmac_f32_e32 v98, v99, v96
	v_fma_f32 v95, -v95, v98, v97
	v_div_fmas_f32 v95, v95, v96, v98
	v_cvt_pk_f32_fp8_e32 v[96:97], v142
	v_div_fixup_f32 v94, v95, v94, 1.0
	v_cvt_pk_f32_fp8_sdwa v[98:99], v142 src0_sel:WORD_1
	s_waitcnt vmcnt(7)
; __device__ __forceinline__ unsigned pk2(float lo, float hi) { const f32x2_t v = {lo, hi}; const bf16x2_t b = __builtin_convertvector(v, bf16x2_t); return __builtin_bit_cast(unsigned, b); }
; __device__ __forceinline__ unsigned pk_fp8x4(float a, float b, float c, float d) { int p = __builtin_amdgcn_cvt_pk_fp8_f32(sat8(a), sat8(b), 0, false); p = __builtin_amdgcn_cvt_pk_fp8_f32(sat8(c), sat8(d), p, true); return (unsigned)p; }
; __device__ __forceinline__ float siluf_(float x) { return x * __builtin_amdgcn_rcpf(1.0f + __expf(-x)); }
; __device__ __forceinline__ void merge_phase(const bf16_t* atto, const float* lse, const bf16_t* ob, const float* ssq, const bf16_t* proj, const float* gla_gain, bf16_t* ya, bf16_t* yb,
;                                             int vcu, int G, int wave, int lane) {
;     ...
;             for (int c = 0; c < 2; ++c) { const int col = 8 * lane + 512 * c;
;                 const f32x4 s0 = sq[r][c][0], s1 = sq[r][c][1], s2 = sq[r][c][2], s3 = sq[r][c][3];
;                 const float tot = ((s0[0] + s0[1]) + (s0[2] + s0[3])) + ((s1[0] + s1[1]) + (s1[2] + s1[3])) + ((s2[0] + s2[1]) + (s2[2] + s2[3])) + ((s3[0] + s3[1]) + (s3[2] + s3[3]));
;                 const float rstd = 1.0f / sqrtf(tot * (1.0f / 256.0f) + NORM_EPS);
;                 const u32x4 ov = o[r][c], rv = rr_[r][c]; u32x4 y; float rf[8];
;     ...
;                 unpack_fp8x8((u32x2){rv.x, rv.y}, rf);
;     ...
;                 rf[0] = bflo(rv.x); rf[1] = bfhi(rv.x); rf[2] = bflo(rv.y); rf[3] = bfhi(rv.y); rf[4] = bflo(rv.z); rf[5] = bfhi(rv.z); rf[6] = bflo(rv.w); rf[7] = bfhi(rv.w);
;     ...
;                 y.x = pk2(bflo(ov.x) * rstd * g0[c][0] * siluf_(rf[0]), bfhi(ov.x) * rstd * g0[c][1] * siluf_(rf[1]));
;                 y.y = pk2(bflo(ov.y) * rstd * g0[c][2] * siluf_(rf[2]), bfhi(ov.y) * rstd * g0[c][3] * siluf_(rf[3]));
;                 y.z = pk2(bflo(ov.z) * rstd * g1[c][0] * siluf_(rf[4]), bfhi(ov.z) * rstd * g1[c][1] * siluf_(rf[5]));
;                 y.w = pk2(bflo(ov.w) * rstd * g1[c][2] * siluf_(rf[6]), bfhi(ov.w) * rstd * g1[c][3] * siluf_(rf[7]));
;     ...
;                 { u32x2 y8; y8.x = pk_fp8x4(bflo(y.x), bfhi(y.x), bflo(y.y), bfhi(y.y)); y8.y = pk_fp8x4(bflo(y.z), bfhi(y.z), bflo(y.w), bfhi(y.w)); *(u32x2*)((unsigned char*)(BR_FUSE ? ya : yb) + (size_t)row * (BR_FUSE ? 1536 : 1024) + col) = y8; }
	v_cvt_pk_f32_fp8_e32 v[48:49], v139
	v_mul_f32_e32 v95, 0xbfb8aa3b, v96
	v_exp_f32_e32 v95, v95
	v_mul_f32_e32 v90, 0xbfb8aa3b, v98
	v_exp_f32_e32 v90, v90
	s_waitcnt vmcnt(4)
	v_add_f32_e32 v24, v24, v25
	v_add_f32_e32 v95, 1.0, v95
	v_rcp_f32_e32 v104, v95
	v_mul_f32_e32 v95, 0xbfb8aa3b, v97
	v_exp_f32_e32 v95, v95
	v_add_f32_e32 v90, 1.0, v90
	v_add_f32_e32 v26, v26, v27
	v_mov_b32_e32 v25, v22
	v_add_f32_e32 v95, 1.0, v95
	v_rcp_f32_e32 v105, v95
	v_pk_mul_f32 v[106:107], v[94:95], v[106:107] op_sel_hi:[0,1]
	v_pk_mul_f32 v[106:107], v[8:9], v[106:107]
	v_mov_b32_e32 v27, v23
	v_pk_mul_f32 v[96:97], v[96:97], v[104:105]
	v_pk_add_f32 v[22:23], v[24:25], v[26:27]
	v_pk_mul_f32 v[96:97], v[106:107], v[96:97]
	s_waitcnt vmcnt(1)
	v_cvt_pk_f32_fp8_e32 v[26:27], v137
	v_cvt_pk_bf16_f32 v104, v96, v97
	v_rcp_f32_e32 v96, v90
	v_mul_f32_e32 v90, 0xbfb8aa3b, v99
	v_exp_f32_e32 v90, v90
	v_lshl_add_u64 v[122:123], v[122:123], 0, s[10:11]
	v_add_f32_e32 v90, 1.0, v90
	v_rcp_f32_e32 v97, v90
	v_lshlrev_b32_e32 v90, 16, v91
	v_and_b32_e32 v91, 0xffff0000, v91
	v_pk_mul_f32 v[90:91], v[94:95], v[90:91] op_sel_hi:[0,1]
	v_pk_mul_f32 v[90:91], v[10:11], v[90:91]
	v_pk_mul_f32 v[96:97], v[98:99], v[96:97]
	s_nop 0
	v_pk_mul_f32 v[90:91], v[90:91], v[96:97]
	v_lshlrev_b32_e32 v96, 16, v92
	v_cvt_pk_bf16_f32 v98, v90, v91
	v_mul_f32_e32 v90, 0xbfb8aa3b, v100
	v_mul_f32_e32 v91, 0xbfb8aa3b, v101
	v_exp_f32_e32 v90, v90
	v_exp_f32_e32 v91, v91
	v_and_b32_e32 v97, 0xffff0000, v92
	v_pk_mul_f32 v[96:97], v[94:95], v[96:97] op_sel_hi:[0,1]
	v_add_f32_e32 v90, 1.0, v90
	v_add_f32_e32 v91, 1.0, v91
	v_rcp_f32_e32 v90, v90
	v_rcp_f32_e32 v91, v91
	v_pk_mul_f32 v[96:97], v[12:13], v[96:97]
	v_lshlrev_b32_e32 v92, 16, v93
	v_and_b32_e32 v93, 0xffff0000, v93
	v_pk_mul_f32 v[90:91], v[100:101], v[90:91]
	v_pk_mul_f32 v[92:93], v[94:95], v[92:93] op_sel_hi:[0,1]
	v_pk_mul_f32 v[90:91], v[96:97], v[90:91]
	v_pk_mul_f32 v[92:93], v[14:15], v[92:93]
	v_cvt_pk_bf16_f32 v90, v90, v91
	v_mul_f32_e32 v91, 0xbfb8aa3b, v102
	v_exp_f32_e32 v91, v91
	s_nop 0
	v_add_f32_e32 v91, 1.0, v91
	v_rcp_f32_e32 v96, v91
	v_mul_f32_e32 v91, 0xbfb8aa3b, v103
	v_exp_f32_e32 v91, v91
	s_nop 0
	v_add_f32_e32 v91, 1.0, v91
	v_rcp_f32_e32 v97, v91
	s_nop 0
	v_pk_mul_f32 v[94:95], v[102:103], v[96:97]
	s_nop 0
	v_pk_mul_f32 v[92:93], v[92:93], v[94:95]
	v_lshlrev_b32_e32 v94, 16, v104
	v_and_b32_e32 v95, 0xffff0000, v104
	v_med3_f32 v94, v94, s70, v190
	v_med3_f32 v95, v95, s70, v190
	v_mov_b32_e32 v96, v33
	v_cvt_pk_fp8_f32 v96, v94, v95
	v_cvt_pk_bf16_f32 v91, v92, v93
	v_lshlrev_b32_e32 v92, 16, v98
	v_and_b32_e32 v93, 0xffff0000, v98
	v_med3_f32 v92, v92, s70, v190
	v_med3_f32 v93, v93, s70, v190
	v_cvt_pk_fp8_f32 v96, v92, v93 op_sel:[0,0,1]
	v_lshlrev_b32_e32 v92, 16, v90
	v_and_b32_e32 v90, 0xffff0000, v90
	v_med3_f32 v92, v92, s70, v190
	v_med3_f32 v90, v90, s70, v190
	v_mov_b32_e32 v97, v33
	v_cvt_pk_fp8_f32 v97, v92, v90
	v_lshlrev_b32_e32 v93, 16, v91
	v_and_b32_e32 v91, 0xffff0000, v91
	v_med3_f32 v90, v93, s70, v190
	v_med3_f32 v91, v91, s70, v190
	v_cvt_pk_fp8_f32 v97, v90, v91 op_sel:[0,0,1]
	v_mov_b32_e32 v90, v87
	v_mov_b32_e32 v91, v88
	v_mov_b32_e32 v87, v89
	v_mov_b32_e32 v88, v83
	v_mov_b32_e32 v89, v84
	v_mov_b32_e32 v83, v85
	v_pk_add_f32 v[86:87], v[90:91], v[86:87]
	v_pk_add_f32 v[82:83], v[88:89], v[82:83]
	v_pk_add_f32 v[86:87], v[86:87], v[86:87] op_sel:[0,1] op_sel_hi:[1,0]
	v_pk_add_f32 v[82:83], v[82:83], v[82:83] op_sel:[0,1] op_sel_hi:[1,0]
	v_mov_b32_e32 v87, v74
	v_mov_b32_e32 v83, v75
	v_pk_add_f32 v[74:75], v[86:87], v[82:83]
	v_lshlrev_b32_e32 v86, 16, v70
	v_pk_add_f32 v[74:75], v[74:75], v[76:77]
	v_and_b32_e32 v87, 0xffff0000, v70
	v_add_f32_e32 v74, v74, v75
	v_fmamk_f32 v74, v74, 0x3b800000, v183
	v_cmp_gt_f32_e32 vcc, s83, v74
	v_mul_f32_e32 v75, 0x4f800000, v74
	v_cvt_pk_f32_fp8_sdwa v[82:83], v141 src0_sel:WORD_1
	v_cndmask_b32_e32 v74, v74, v75, vcc
	v_sqrt_f32_e32 v75, v74
	global_store_dwordx2 v[110:111], v[96:97], off
	v_add_u32_e32 v76, -1, v75
	v_fma_f32 v77, -v76, v75, v74
	v_cmp_ge_f32_e64 s[4:5], 0, v77
	v_add_u32_e32 v77, 1, v75
	s_nop 0
	v_cndmask_b32_e64 v76, v75, v76, s[4:5]
	v_fma_f32 v75, -v77, v75, v74
	v_cmp_lt_f32_e64 s[4:5], 0, v75
	s_nop 1
	v_cndmask_b32_e64 v75, v76, v77, s[4:5]
	v_mul_f32_e32 v76, 0x37800000, v75
	v_cndmask_b32_e32 v75, v75, v76, vcc
	v_cmp_class_f32_e32 vcc, v74, v184
	s_nop 1
	v_cndmask_b32_e32 v74, v75, v74, vcc
	v_div_scale_f32 v75, s[2:3], v74, v74, 1.0
	v_rcp_f32_e32 v76, v75
	s_nop 0
	v_fma_f32 v77, -v75, v76, 1.0
	v_fmac_f32_e32 v76, v77, v76
	v_div_scale_f32 v77, vcc, 1.0, v74, 1.0
	v_mul_f32_e32 v78, v77, v76
	v_fma_f32 v79, -v75, v78, v77
	v_fmac_f32_e32 v78, v79, v76
	v_fma_f32 v75, -v75, v78, v77
	v_div_fmas_f32 v75, v75, v76, v78
	v_cvt_pk_f32_fp8_e32 v[76:77], v140
	v_div_fixup_f32 v74, v75, v74, 1.0
	v_cvt_pk_f32_fp8_sdwa v[78:79], v140 src0_sel:WORD_1
	v_mul_f32_e32 v75, 0xbfb8aa3b, v76
	v_exp_f32_e32 v75, v75
	v_mul_f32_e32 v70, 0xbfb8aa3b, v78
	v_exp_f32_e32 v70, v70
	v_add_f32_e32 v75, 1.0, v75
	v_rcp_f32_e32 v84, v75
	v_mul_f32_e32 v75, 0xbfb8aa3b, v77
	v_exp_f32_e32 v75, v75
	v_add_f32_e32 v70, 1.0, v70
	v_add_f32_e32 v75, 1.0, v75
	v_rcp_f32_e32 v85, v75
	v_pk_mul_f32 v[86:87], v[74:75], v[86:87] op_sel_hi:[0,1]
	v_pk_mul_f32 v[86:87], v[0:1], v[86:87]
	v_pk_mul_f32 v[76:77], v[76:77], v[84:85]
	s_nop 0
	v_pk_mul_f32 v[76:77], v[86:87], v[76:77]
	s_nop 0
	v_cvt_pk_bf16_f32 v84, v76, v77
	v_rcp_f32_e32 v76, v70
	v_mul_f32_e32 v70, 0xbfb8aa3b, v79
	v_exp_f32_e32 v70, v70
	s_nop 0
	v_add_f32_e32 v70, 1.0, v70
	v_rcp_f32_e32 v77, v70
	v_lshlrev_b32_e32 v70, 16, v71
	v_and_b32_e32 v71, 0xffff0000, v71
; __device__ __forceinline__ void merge_phase(const bf16_t* atto, const float* lse, const bf16_t* ob, const float* ssq, const bf16_t* proj, const float* gla_gain, bf16_t* ya, bf16_t* yb,
;                                             int vcu, int G, int wave, int lane) {
;     ...
;         for (int r = 0; r < 2; ++r) { const int row = row0 + r;
;             const float m = fmaxf(l0[r], fmaxf(l1[r], l2[r])); float e0 = __expf(l0[r] - m), e1 = __expf(l1[r] - m), e2 = __expf(l2[r] - m); const float inv = 1.0f / (e0 + e1 + e2); e0 *= inv; e1 *= inv; e2 *= inv;
;             u32x4 w;
;             w.x = pk2(e0 * bflo(a0[r].x) + e1 * bflo(a1[r].x) + e2 * bflo(a2[r].x), e0 * bfhi(a0[r].x) + e1 * bfhi(a1[r].x) + e2 * bfhi(a2[r].x));
;             w.y = pk2(e0 * bflo(a0[r].y) + e1 * bflo(a1[r].y) + e2 * bflo(a2[r].y), e0 * bfhi(a0[r].y) + e1 * bfhi(a1[r].y) + e2 * bfhi(a2[r].y));
;             w.z = pk2(e0 * bflo(a0[r].z) + e1 * bflo(a1[r].z) + e2 * bflo(a2[r].z), e0 * bfhi(a0[r].z) + e1 * bfhi(a1[r].z) + e2 * bfhi(a2[r].z));
;             w.w = pk2(e0 * bflo(a0[r].w) + e1 * bflo(a1[r].w) + e2 * bflo(a2[r].w), e0 * bfhi(a0[r].w) + e1 * bfhi(a1[r].w) + e2 * bfhi(a2[r].w));
;     ...
;             { u32x2 w8; w8.x = pk_fp8x4(bflo(w.x), bfhi(w.x), bflo(w.y), bfhi(w.y)); w8.y = pk_fp8x4(bflo(w.z), bfhi(w.z), bflo(w.w), bfhi(w.w)); *(u32x2*)((unsigned char*)ya + (BR_FUSE ? (size_t)row * 1536 + 1024 : (size_t)row * 512) + 8 * lane) = w8; }
;     ...
;             *(u32x4*)(ya + (size_t)row * 512 + 8 * lane) = w;
;     ...
; #pragma unroll
;             for (int c = 0; c < 2; ++c) { const int col = 8 * lane + 512 * c;
;                 const f32x4 s0 = sq[r][c][0], s1 = sq[r][c][1], s2 = sq[r][c][2], s3 = sq[r][c][3];
;                 const float tot = ((s0[0] + s0[1]) + (s0[2] + s0[3])) + ((s1[0] + s1[1]) + (s1[2] + s1[3])) + ((s2[0] + s2[1]) + (s2[2] + s2[3])) + ((s3[0] + s3[1]) + (s3[2] + s3[3]));
;                 const float rstd = 1.0f / sqrtf(tot * (1.0f / 256.0f) + NORM_EPS);
;                 const u32x4 ov = o[r][c], rv = rr_[r][c]; u32x4 y; float rf[8];
;     ...
;                 unpack_fp8x8((u32x2){rv.x, rv.y}, rf);
;     ...
;                 rf[0] = bflo(rv.x); rf[1] = bfhi(rv.x); rf[2] = bflo(rv.y); rf[3] = bfhi(rv.y); rf[4] = bflo(rv.z); rf[5] = bfhi(rv.z); rf[6] = bflo(rv.w); rf[7] = bfhi(rv.w);
	v_pk_mul_f32 v[70:71], v[74:75], v[70:71] op_sel_hi:[0,1]
	v_pk_mul_f32 v[70:71], v[2:3], v[70:71]
	v_pk_mul_f32 v[76:77], v[78:79], v[76:77]
	v_and_b32_e32 v79, 0xffff0000, v58
	v_pk_mul_f32 v[70:71], v[70:71], v[76:77]
	v_lshlrev_b32_e32 v76, 16, v72
	v_cvt_pk_bf16_f32 v78, v70, v71
	v_mul_f32_e32 v70, 0xbfb8aa3b, v80
	v_mul_f32_e32 v71, 0xbfb8aa3b, v81
	v_exp_f32_e32 v70, v70
	v_exp_f32_e32 v71, v71
	v_and_b32_e32 v77, 0xffff0000, v72
	v_pk_mul_f32 v[76:77], v[74:75], v[76:77] op_sel_hi:[0,1]
	v_add_f32_e32 v70, 1.0, v70
	v_add_f32_e32 v71, 1.0, v71
	v_rcp_f32_e32 v70, v70
	v_rcp_f32_e32 v71, v71
	v_pk_mul_f32 v[76:77], v[4:5], v[76:77]
	v_lshlrev_b32_e32 v72, 16, v73
	v_and_b32_e32 v73, 0xffff0000, v73
	v_pk_mul_f32 v[70:71], v[80:81], v[70:71]
	v_pk_mul_f32 v[72:73], v[74:75], v[72:73] op_sel_hi:[0,1]
	v_pk_mul_f32 v[70:71], v[76:77], v[70:71]
	v_pk_mul_f32 v[72:73], v[6:7], v[72:73]
	v_cvt_pk_bf16_f32 v70, v70, v71
	v_mul_f32_e32 v71, 0xbfb8aa3b, v82
	v_exp_f32_e32 v71, v71
	s_nop 0
	v_add_f32_e32 v71, 1.0, v71
	v_rcp_f32_e32 v76, v71
	v_mul_f32_e32 v71, 0xbfb8aa3b, v83
	v_exp_f32_e32 v71, v71
	s_nop 0
	v_add_f32_e32 v71, 1.0, v71
	v_rcp_f32_e32 v77, v71
	s_nop 0
	v_pk_mul_f32 v[74:75], v[82:83], v[76:77]
	s_nop 0
	v_pk_mul_f32 v[72:73], v[72:73], v[74:75]
	v_lshlrev_b32_e32 v74, 16, v84
	v_and_b32_e32 v75, 0xffff0000, v84
	v_med3_f32 v74, v74, s70, v190
	v_med3_f32 v75, v75, s70, v190
	v_mov_b32_e32 v76, v33
	v_cvt_pk_fp8_f32 v76, v74, v75
	v_cvt_pk_bf16_f32 v71, v72, v73
	v_lshlrev_b32_e32 v72, 16, v78
	v_and_b32_e32 v73, 0xffff0000, v78
	v_med3_f32 v72, v72, s70, v190
	v_med3_f32 v73, v73, s70, v190
	v_cvt_pk_fp8_f32 v76, v72, v73 op_sel:[0,0,1]
	v_lshlrev_b32_e32 v72, 16, v70
	v_and_b32_e32 v70, 0xffff0000, v70
	v_med3_f32 v72, v72, s70, v190
	v_med3_f32 v70, v70, s70, v190
	v_mov_b32_e32 v77, v33
	v_cvt_pk_fp8_f32 v77, v72, v70
	v_lshlrev_b32_e32 v73, 16, v71
	v_and_b32_e32 v71, 0xffff0000, v71
	v_med3_f32 v70, v73, s70, v190
	v_med3_f32 v71, v71, s70, v190
	v_max3_f32 v72, v145, v144, v32
	v_cvt_pk_fp8_f32 v77, v70, v71 op_sel:[0,0,1]
	v_sub_f32_e32 v70, v145, v72
	v_mul_f32_e32 v70, 0x3fb8aa3b, v70
	v_exp_f32_e32 v71, v70
	v_sub_f32_e32 v70, v144, v72
	v_mul_f32_e32 v70, 0x3fb8aa3b, v70
	v_sub_f32_e32 v32, v32, v72
	v_exp_f32_e32 v70, v70
	v_mul_f32_e32 v32, 0x3fb8aa3b, v32
	v_exp_f32_e32 v72, v32
	global_store_dwordx2 v[110:111], v[76:77], off offset:512
	v_add_f32_e32 v32, v71, v70
	v_lshlrev_b32_e32 v78, 16, v58
	v_add_f32_e32 v32, v72, v32
	v_div_scale_f32 v73, s[2:3], v32, v32, 1.0
	v_rcp_f32_e32 v74, v73
	v_lshlrev_b32_e32 v58, 16, v59
	v_and_b32_e32 v59, 0xffff0000, v59
	v_fma_f32 v75, -v73, v74, 1.0
	v_fmac_f32_e32 v74, v75, v74
	v_div_scale_f32 v75, vcc, 1.0, v32, 1.0
	v_mul_f32_e32 v76, v75, v74
	v_fma_f32 v77, -v73, v76, v75
	v_fmac_f32_e32 v76, v77, v74
	v_fma_f32 v73, -v73, v76, v75
	v_div_fmas_f32 v73, v73, v74, v76
	v_div_fixup_f32 v32, v73, v32, 1.0
	v_pk_mul_f32 v[70:71], v[70:71], v[32:33] op_sel_hi:[1,0]
	v_lshlrev_b32_e32 v76, 16, v62
	v_and_b32_e32 v77, 0xffff0000, v66
	v_lshlrev_b32_e32 v74, 16, v66
	v_and_b32_e32 v75, 0xffff0000, v62
	v_pk_mul_f32 v[76:77], v[70:71], v[76:77] op_sel:[1,0] op_sel_hi:[0,1]
	v_mul_f32_e32 v72, v72, v32
	v_pk_fma_f32 v[74:75], v[70:71], v[74:75], v[76:77]
	v_lshlrev_b32_e32 v62, 16, v63
	v_pk_fma_f32 v[74:75], v[72:73], v[78:79], v[74:75] op_sel_hi:[0,1,1]
	v_cvt_pk_bf16_f32 v32, v74, v75
	v_and_b32_e32 v75, 0xffff0000, v63
	v_and_b32_e32 v63, 0xffff0000, v67
	v_lshlrev_b32_e32 v74, 16, v67
	v_pk_mul_f32 v[62:63], v[70:71], v[62:63] op_sel:[1,0] op_sel_hi:[0,1]
	v_pk_fma_f32 v[62:63], v[70:71], v[74:75], v[62:63]
	v_lshlrev_b32_e32 v66, 16, v60
	v_pk_fma_f32 v[58:59], v[72:73], v[58:59], v[62:63] op_sel_hi:[0,1,1]
	v_lshlrev_b32_e32 v62, 16, v64
	v_and_b32_e32 v63, 0xffff0000, v68
	v_cvt_pk_bf16_f32 v73, v58, v59
	v_lshlrev_b32_e32 v58, 16, v68
	v_and_b32_e32 v59, 0xffff0000, v64
	v_pk_mul_f32 v[62:63], v[70:71], v[62:63] op_sel:[1,0] op_sel_hi:[0,1]
	v_and_b32_e32 v67, 0xffff0000, v60
	v_pk_fma_f32 v[58:59], v[70:71], v[58:59], v[62:63]
	v_lshlrev_b32_e32 v62, 16, v65
	v_pk_fma_f32 v[58:59], v[72:73], v[66:67], v[58:59] op_sel_hi:[0,1,1]
	v_and_b32_e32 v63, 0xffff0000, v69
	v_cvt_pk_bf16_f32 v64, v58, v59
	v_lshlrev_b32_e32 v58, 16, v69
	v_and_b32_e32 v59, 0xffff0000, v65
	v_pk_mul_f32 v[62:63], v[70:71], v[62:63] op_sel:[1,0] op_sel_hi:[0,1]
	v_pk_fma_f32 v[58:59], v[70:71], v[58:59], v[62:63]
	v_lshlrev_b32_e32 v60, 16, v61
	v_and_b32_e32 v61, 0xffff0000, v61
	v_pk_fma_f32 v[58:59], v[72:73], v[60:61], v[58:59] op_sel_hi:[0,1,1]
	v_cvt_pk_bf16_f32 v59, v58, v59
	v_lshlrev_b32_e32 v58, 16, v32
	v_and_b32_e32 v32, 0xffff0000, v32
	v_med3_f32 v62, v58, s70, v190
	v_med3_f32 v32, v32, s70, v190
	v_mov_b32_e32 v58, v33
	v_cvt_pk_fp8_f32 v58, v62, v32
	v_lshlrev_b32_e32 v60, 16, v73
	v_and_b32_e32 v61, 0xffff0000, v73
	v_med3_f32 v32, v60, s70, v190
	v_med3_f32 v60, v61, s70, v190
	v_cvt_pk_fp8_f32 v58, v32, v60 op_sel:[0,0,1]
	v_lshlrev_b32_e32 v32, 16, v64
	v_and_b32_e32 v60, 0xffff0000, v64
	v_lshlrev_b32_e32 v61, 16, v59
	v_and_b32_e32 v62, 0xffff0000, v59
	v_med3_f32 v32, v32, s70, v190
	v_med3_f32 v60, v60, s70, v190
	v_mov_b32_e32 v59, v33
	v_cvt_pk_fp8_f32 v59, v32, v60
	v_med3_f32 v32, v61, s70, v190
	v_med3_f32 v60, v62, s70, v190
	v_cvt_pk_fp8_f32 v59, v32, v60 op_sel:[0,0,1]
	global_store_dwordx2 v[110:111], v[58:59], off offset:2560
	v_mov_b32_e32 v58, v55
	v_mov_b32_e32 v59, v56
	v_mov_b32_e32 v55, v57
	v_mov_b32_e32 v56, v51
	v_mov_b32_e32 v57, v52
	v_mov_b32_e32 v51, v53
	v_pk_add_f32 v[54:55], v[58:59], v[54:55]
	v_pk_add_f32 v[50:51], v[56:57], v[50:51]
; __device__ __forceinline__ unsigned pk2(float lo, float hi) { const f32x2_t v = {lo, hi}; const bf16x2_t b = __builtin_convertvector(v, bf16x2_t); return __builtin_bit_cast(unsigned, b); }
; __device__ __forceinline__ unsigned pk_fp8x4(float a, float b, float c, float d) { int p = __builtin_amdgcn_cvt_pk_fp8_f32(sat8(a), sat8(b), 0, false); p = __builtin_amdgcn_cvt_pk_fp8_f32(sat8(c), sat8(d), p, true); return (unsigned)p; }
; __device__ __forceinline__ float siluf_(float x) { return x * __builtin_amdgcn_rcpf(1.0f + __expf(-x)); }
; __device__ __forceinline__ void merge_phase(const bf16_t* atto, const float* lse, const bf16_t* ob, const float* ssq, const bf16_t* proj, const float* gla_gain, bf16_t* ya, bf16_t* yb,
;                                             int vcu, int G, int wave, int lane) {
;     ...
;             for (int c = 0; c < 2; ++c) { const int col = 8 * lane + 512 * c;
;                 const f32x4 s0 = sq[r][c][0], s1 = sq[r][c][1], s2 = sq[r][c][2], s3 = sq[r][c][3];
;                 const float tot = ((s0[0] + s0[1]) + (s0[2] + s0[3])) + ((s1[0] + s1[1]) + (s1[2] + s1[3])) + ((s2[0] + s2[1]) + (s2[2] + s2[3])) + ((s3[0] + s3[1]) + (s3[2] + s3[3]));
;                 const float rstd = 1.0f / sqrtf(tot * (1.0f / 256.0f) + NORM_EPS);
;                 const u32x4 ov = o[r][c], rv = rr_[r][c]; u32x4 y; float rf[8];
;     ...
;                 unpack_fp8x8((u32x2){rv.x, rv.y}, rf);
;     ...
;                 rf[0] = bflo(rv.x); rf[1] = bfhi(rv.x); rf[2] = bflo(rv.y); rf[3] = bfhi(rv.y); rf[4] = bflo(rv.z); rf[5] = bfhi(rv.z); rf[6] = bflo(rv.w); rf[7] = bfhi(rv.w);
;     ...
;                 y.x = pk2(bflo(ov.x) * rstd * g0[c][0] * siluf_(rf[0]), bfhi(ov.x) * rstd * g0[c][1] * siluf_(rf[1]));
;                 y.y = pk2(bflo(ov.y) * rstd * g0[c][2] * siluf_(rf[2]), bfhi(ov.y) * rstd * g0[c][3] * siluf_(rf[3]));
;                 y.z = pk2(bflo(ov.z) * rstd * g1[c][0] * siluf_(rf[4]), bfhi(ov.z) * rstd * g1[c][1] * siluf_(rf[5]));
;                 y.w = pk2(bflo(ov.w) * rstd * g1[c][2] * siluf_(rf[6]), bfhi(ov.w) * rstd * g1[c][3] * siluf_(rf[7]));
;     ...
;                 { u32x2 y8; y8.x = pk_fp8x4(bflo(y.x), bfhi(y.x), bflo(y.y), bfhi(y.y)); y8.y = pk_fp8x4(bflo(y.z), bfhi(y.z), bflo(y.w), bfhi(y.w)); *(u32x2*)((unsigned char*)(BR_FUSE ? ya : yb) + (size_t)row * (BR_FUSE ? 1536 : 1024) + col) = y8; }
	v_pk_add_f32 v[54:55], v[54:55], v[54:55] op_sel:[0,1] op_sel_hi:[1,0]
	v_pk_add_f32 v[50:51], v[50:51], v[50:51] op_sel:[0,1] op_sel_hi:[1,0]
	v_mov_b32_e32 v55, v42
	v_mov_b32_e32 v51, v43
	v_pk_add_f32 v[42:43], v[54:55], v[50:51]
	v_lshlrev_b32_e32 v54, 16, v38
	v_pk_add_f32 v[42:43], v[42:43], v[44:45]
	v_and_b32_e32 v55, 0xffff0000, v38
	v_add_f32_e32 v32, v42, v43
	v_fmamk_f32 v32, v32, 0x3b800000, v183
	v_cmp_gt_f32_e32 vcc, s83, v32
	v_mul_f32_e32 v42, 0x4f800000, v32
	v_lshlrev_b32_e32 v38, 16, v39
	v_cndmask_b32_e32 v32, v32, v42, vcc
	v_sqrt_f32_e32 v42, v32
	v_and_b32_e32 v39, 0xffff0000, v39
	v_cvt_pk_f32_fp8_sdwa v[50:51], v139 src0_sel:WORD_1
	v_add_u32_e32 v43, -1, v42
	v_fma_f32 v44, -v43, v42, v32
	v_cmp_ge_f32_e64 s[4:5], 0, v44
	v_add_u32_e32 v44, 1, v42
	s_nop 0
	v_cndmask_b32_e64 v43, v42, v43, s[4:5]
	v_fma_f32 v42, -v44, v42, v32
	v_cmp_lt_f32_e64 s[4:5], 0, v42
	s_nop 1
	v_cndmask_b32_e64 v42, v43, v44, s[4:5]
	v_mul_f32_e32 v43, 0x37800000, v42
	v_cndmask_b32_e32 v42, v42, v43, vcc
	v_cmp_class_f32_e32 vcc, v32, v184
	s_nop 1
	v_cndmask_b32_e32 v32, v42, v32, vcc
	v_div_scale_f32 v42, s[2:3], v32, v32, 1.0
	v_rcp_f32_e32 v43, v42
	s_nop 0
	v_fma_f32 v44, -v42, v43, 1.0
	v_fmac_f32_e32 v43, v44, v43
	v_div_scale_f32 v44, vcc, 1.0, v32, 1.0
	v_mul_f32_e32 v45, v44, v43
	v_fma_f32 v46, -v42, v45, v44
	v_fmac_f32_e32 v45, v46, v43
	v_fma_f32 v42, -v42, v45, v44
	v_div_fmas_f32 v42, v42, v43, v45
	v_cvt_pk_f32_fp8_e32 v[44:45], v138
	v_div_fixup_f32 v42, v42, v32, 1.0
	v_cvt_pk_f32_fp8_sdwa v[46:47], v138 src0_sel:WORD_1
	v_pk_mul_f32 v[54:55], v[42:43], v[54:55] op_sel_hi:[0,1]
	v_mul_f32_e32 v32, 0xbfb8aa3b, v44
	v_exp_f32_e32 v32, v32
	v_pk_mul_f32 v[54:55], v[8:9], v[54:55]
	v_add_f32_e32 v32, 1.0, v32
	v_rcp_f32_e32 v52, v32
	v_mul_f32_e32 v32, 0xbfb8aa3b, v45
	v_exp_f32_e32 v32, v32
	s_nop 0
	v_add_f32_e32 v32, 1.0, v32
	v_rcp_f32_e32 v53, v32
	v_mul_f32_e32 v32, 0xbfb8aa3b, v46
	v_exp_f32_e32 v32, v32
	v_pk_mul_f32 v[44:45], v[44:45], v[52:53]
	s_nop 0
	v_pk_mul_f32 v[44:45], v[54:55], v[44:45]
	v_add_f32_e32 v32, 1.0, v32
	v_cvt_pk_bf16_f32 v43, v44, v45
	v_rcp_f32_e32 v44, v32
	v_mul_f32_e32 v32, 0xbfb8aa3b, v47
	v_exp_f32_e32 v32, v32
	v_pk_mul_f32 v[38:39], v[42:43], v[38:39] op_sel_hi:[0,1]
	v_pk_mul_f32 v[38:39], v[10:11], v[38:39]
	v_add_f32_e32 v32, 1.0, v32
	v_rcp_f32_e32 v45, v32
	v_mul_f32_e32 v32, 0xbfb8aa3b, v48
	v_exp_f32_e32 v32, v32
	v_pk_mul_f32 v[44:45], v[46:47], v[44:45]
	s_nop 0
	v_pk_mul_f32 v[38:39], v[38:39], v[44:45]
	v_add_f32_e32 v32, 1.0, v32
	v_cvt_pk_bf16_f32 v46, v38, v39
	v_rcp_f32_e32 v38, v32
	v_mul_f32_e32 v32, 0xbfb8aa3b, v49
	v_exp_f32_e32 v32, v32
	v_lshlrev_b32_e32 v44, 16, v40
	v_and_b32_e32 v45, 0xffff0000, v40
	v_pk_mul_f32 v[44:45], v[42:43], v[44:45] op_sel_hi:[0,1]
	v_add_f32_e32 v32, 1.0, v32
	v_rcp_f32_e32 v39, v32
	v_pk_mul_f32 v[44:45], v[12:13], v[44:45]
	v_lshlrev_b32_e32 v40, 16, v41
	v_and_b32_e32 v41, 0xffff0000, v41
	v_pk_mul_f32 v[38:39], v[48:49], v[38:39]
	v_pk_mul_f32 v[40:41], v[42:43], v[40:41] op_sel_hi:[0,1]
	v_pk_mul_f32 v[38:39], v[44:45], v[38:39]
	v_pk_mul_f32 v[40:41], v[14:15], v[40:41]
	v_cvt_pk_bf16_f32 v32, v38, v39
	v_mul_f32_e32 v38, 0xbfb8aa3b, v50
	v_mul_f32_e32 v39, 0xbfb8aa3b, v51
	v_exp_f32_e32 v38, v38
	v_exp_f32_e32 v39, v39
	v_and_b32_e32 v42, 0xffff0000, v43
	v_med3_f32 v42, v42, s70, v190
	v_add_f32_e32 v38, 1.0, v38
	v_add_f32_e32 v39, 1.0, v39
	v_rcp_f32_e32 v38, v38
	v_rcp_f32_e32 v39, v39
	v_mov_b32_e32 v44, v33
	v_mov_b32_e32 v45, v33
	v_pk_mul_f32 v[38:39], v[50:51], v[38:39]
	s_nop 0
	v_pk_mul_f32 v[38:39], v[40:41], v[38:39]
	v_lshlrev_b32_e32 v41, 16, v43
	v_med3_f32 v41, v41, s70, v190
	v_cvt_pk_fp8_f32 v44, v41, v42
	v_cvt_pk_bf16_f32 v38, v38, v39
	v_lshlrev_b32_e32 v39, 16, v46
	v_and_b32_e32 v40, 0xffff0000, v46
	v_med3_f32 v39, v39, s70, v190
	v_med3_f32 v40, v40, s70, v190
	v_cvt_pk_fp8_f32 v44, v39, v40 op_sel:[0,0,1]
	v_lshlrev_b32_e32 v39, 16, v32
	v_and_b32_e32 v32, 0xffff0000, v32
	v_med3_f32 v39, v39, s70, v190
	v_med3_f32 v32, v32, s70, v190
	v_cvt_pk_fp8_f32 v45, v39, v32
	v_lshlrev_b32_e32 v40, 16, v38
	v_and_b32_e32 v38, 0xffff0000, v38
	v_med3_f32 v32, v40, s70, v190
	v_med3_f32 v38, v38, s70, v190
	v_cvt_pk_fp8_f32 v45, v32, v38 op_sel:[0,0,1]
	v_mov_b32_e32 v38, v35
	v_mov_b32_e32 v39, v36
	v_mov_b32_e32 v35, v37
	v_mov_b32_e32 v36, v29
	v_mov_b32_e32 v37, v30
	v_mov_b32_e32 v29, v31
	v_pk_add_f32 v[34:35], v[38:39], v[34:35]
; __device__ __forceinline__ unsigned pk2(float lo, float hi) { const f32x2_t v = {lo, hi}; const bf16x2_t b = __builtin_convertvector(v, bf16x2_t); return __builtin_bit_cast(unsigned, b); }
; __device__ __forceinline__ unsigned pk_fp8x4(float a, float b, float c, float d) { int p = __builtin_amdgcn_cvt_pk_fp8_f32(sat8(a), sat8(b), 0, false); p = __builtin_amdgcn_cvt_pk_fp8_f32(sat8(c), sat8(d), p, true); return (unsigned)p; }
; __device__ __forceinline__ float siluf_(float x) { return x * __builtin_amdgcn_rcpf(1.0f + __expf(-x)); }
; __device__ __forceinline__ void merge_phase(const bf16_t* atto, const float* lse, const bf16_t* ob, const float* ssq, const bf16_t* proj, const float* gla_gain, bf16_t* ya, bf16_t* yb,
;                                             int vcu, int G, int wave, int lane) {
;     ...
;             for (int c = 0; c < 2; ++c) { const int col = 8 * lane + 512 * c;
;                 const f32x4 s0 = sq[r][c][0], s1 = sq[r][c][1], s2 = sq[r][c][2], s3 = sq[r][c][3];
;                 const float tot = ((s0[0] + s0[1]) + (s0[2] + s0[3])) + ((s1[0] + s1[1]) + (s1[2] + s1[3])) + ((s2[0] + s2[1]) + (s2[2] + s2[3])) + ((s3[0] + s3[1]) + (s3[2] + s3[3]));
;                 const float rstd = 1.0f / sqrtf(tot * (1.0f / 256.0f) + NORM_EPS);
;                 const u32x4 ov = o[r][c], rv = rr_[r][c]; u32x4 y; float rf[8];
;     ...
;                 unpack_fp8x8((u32x2){rv.x, rv.y}, rf);
;     ...
;                 rf[0] = bflo(rv.x); rf[1] = bfhi(rv.x); rf[2] = bflo(rv.y); rf[3] = bfhi(rv.y); rf[4] = bflo(rv.z); rf[5] = bfhi(rv.z); rf[6] = bflo(rv.w); rf[7] = bfhi(rv.w);
;     ...
;                 y.x = pk2(bflo(ov.x) * rstd * g0[c][0] * siluf_(rf[0]), bfhi(ov.x) * rstd * g0[c][1] * siluf_(rf[1]));
;                 y.y = pk2(bflo(ov.y) * rstd * g0[c][2] * siluf_(rf[2]), bfhi(ov.y) * rstd * g0[c][3] * siluf_(rf[3]));
;                 y.z = pk2(bflo(ov.z) * rstd * g1[c][0] * siluf_(rf[4]), bfhi(ov.z) * rstd * g1[c][1] * siluf_(rf[5]));
;                 y.w = pk2(bflo(ov.w) * rstd * g1[c][2] * siluf_(rf[6]), bfhi(ov.w) * rstd * g1[c][3] * siluf_(rf[7]));
;     ...
;                 { u32x2 y8; y8.x = pk_fp8x4(bflo(y.x), bfhi(y.x), bflo(y.y), bfhi(y.y)); y8.y = pk_fp8x4(bflo(y.z), bfhi(y.z), bflo(y.w), bfhi(y.w)); *(u32x2*)((unsigned char*)(BR_FUSE ? ya : yb) + (size_t)row * (BR_FUSE ? 1536 : 1024) + col) = y8; }
;     ...
;                 *(u32x4*)(yb + (size_t)row * 1024 + col) = y;
;     ...
;             } }
	v_pk_add_f32 v[28:29], v[36:37], v[28:29]
	v_pk_add_f32 v[34:35], v[34:35], v[34:35] op_sel:[0,1] op_sel_hi:[1,0]
	v_pk_add_f32 v[28:29], v[28:29], v[28:29] op_sel:[0,1] op_sel_hi:[1,0]
	v_mov_b32_e32 v35, v20
	v_mov_b32_e32 v29, v21
	v_pk_add_f32 v[20:21], v[34:35], v[28:29]
	v_lshlrev_b32_e32 v34, 16, v16
	v_pk_add_f32 v[20:21], v[20:21], v[22:23]
	v_and_b32_e32 v35, 0xffff0000, v16
	v_add_f32_e32 v20, v20, v21
	v_fmamk_f32 v20, v20, 0x3b800000, v183
	v_cmp_gt_f32_e32 vcc, s83, v20
	v_mul_f32_e32 v21, 0x4f800000, v20
	v_cvt_pk_f32_fp8_sdwa v[28:29], v137 src0_sel:WORD_1
	v_cndmask_b32_e32 v20, v20, v21, vcc
	v_sqrt_f32_e32 v21, v20
	global_store_dwordx2 v[110:111], v[44:45], off offset:1536
	v_add_u32_e32 v22, -1, v21
	v_fma_f32 v23, -v22, v21, v20
	v_cmp_ge_f32_e64 s[4:5], 0, v23
	v_add_u32_e32 v23, 1, v21
	s_nop 0
	v_cndmask_b32_e64 v22, v21, v22, s[4:5]
	v_fma_f32 v21, -v23, v21, v20
	v_cmp_lt_f32_e64 s[4:5], 0, v21
	s_nop 1
	v_cndmask_b32_e64 v21, v22, v23, s[4:5]
	v_mul_f32_e32 v22, 0x37800000, v21
	v_cndmask_b32_e32 v21, v21, v22, vcc
	v_cmp_class_f32_e32 vcc, v20, v184
	s_nop 1
	v_cndmask_b32_e32 v20, v21, v20, vcc
	v_div_scale_f32 v21, s[2:3], v20, v20, 1.0
	v_rcp_f32_e32 v22, v21
	s_nop 0
	v_fma_f32 v23, -v21, v22, 1.0
	v_fmac_f32_e32 v22, v23, v22
	v_div_scale_f32 v23, vcc, 1.0, v20, 1.0
	v_mul_f32_e32 v24, v23, v22
	v_fma_f32 v25, -v21, v24, v23
	v_fmac_f32_e32 v24, v25, v22
	v_fma_f32 v21, -v21, v24, v23
	v_div_fmas_f32 v21, v21, v22, v24
	v_cvt_pk_f32_fp8_e32 v[22:23], v136
	v_div_fixup_f32 v20, v21, v20, 1.0
	v_cvt_pk_f32_fp8_sdwa v[24:25], v136 src0_sel:WORD_1
	v_mul_f32_e32 v21, 0xbfb8aa3b, v22
	v_exp_f32_e32 v21, v21
	v_mul_f32_e32 v16, 0xbfb8aa3b, v24
	v_exp_f32_e32 v16, v16
	v_add_f32_e32 v21, 1.0, v21
	v_rcp_f32_e32 v30, v21
	v_mul_f32_e32 v21, 0xbfb8aa3b, v23
	v_exp_f32_e32 v21, v21
	v_add_f32_e32 v16, 1.0, v16
	v_add_f32_e32 v21, 1.0, v21
	v_rcp_f32_e32 v31, v21
	v_pk_mul_f32 v[34:35], v[20:21], v[34:35] op_sel_hi:[0,1]
	v_pk_mul_f32 v[34:35], v[0:1], v[34:35]
	v_pk_mul_f32 v[22:23], v[22:23], v[30:31]
	s_nop 0
	v_pk_mul_f32 v[22:23], v[34:35], v[22:23]
	s_nop 0
	v_cvt_pk_bf16_f32 v30, v22, v23
	v_rcp_f32_e32 v22, v16
	v_mul_f32_e32 v16, 0xbfb8aa3b, v25
	v_exp_f32_e32 v16, v16
	s_nop 0
	v_add_f32_e32 v16, 1.0, v16
	v_rcp_f32_e32 v23, v16
	v_lshlrev_b32_e32 v16, 16, v17
	v_and_b32_e32 v17, 0xffff0000, v17
	v_pk_mul_f32 v[16:17], v[20:21], v[16:17] op_sel_hi:[0,1]
	v_pk_mul_f32 v[16:17], v[2:3], v[16:17]
	v_pk_mul_f32 v[22:23], v[24:25], v[22:23]
	s_nop 0
	v_pk_mul_f32 v[16:17], v[16:17], v[22:23]
	v_lshlrev_b32_e32 v22, 16, v18
	v_cvt_pk_bf16_f32 v24, v16, v17
	v_mul_f32_e32 v16, 0xbfb8aa3b, v26
	v_mul_f32_e32 v17, 0xbfb8aa3b, v27
	v_exp_f32_e32 v16, v16
	v_exp_f32_e32 v17, v17
	v_and_b32_e32 v23, 0xffff0000, v18
	v_pk_mul_f32 v[22:23], v[20:21], v[22:23] op_sel_hi:[0,1]
	v_add_f32_e32 v16, 1.0, v16
	v_add_f32_e32 v17, 1.0, v17
	v_rcp_f32_e32 v16, v16
	v_rcp_f32_e32 v17, v17
	v_pk_mul_f32 v[22:23], v[4:5], v[22:23]
	v_lshlrev_b32_e32 v18, 16, v19
	v_and_b32_e32 v19, 0xffff0000, v19
	v_pk_mul_f32 v[16:17], v[26:27], v[16:17]
	v_pk_mul_f32 v[18:19], v[20:21], v[18:19] op_sel_hi:[0,1]
	v_pk_mul_f32 v[16:17], v[22:23], v[16:17]
	v_pk_mul_f32 v[18:19], v[6:7], v[18:19]
	v_cvt_pk_bf16_f32 v16, v16, v17
	v_mul_f32_e32 v17, 0xbfb8aa3b, v28
	v_exp_f32_e32 v17, v17
	s_nop 0
	v_add_f32_e32 v17, 1.0, v17
	v_rcp_f32_e32 v22, v17
	v_mul_f32_e32 v17, 0xbfb8aa3b, v29
	v_exp_f32_e32 v17, v17
	s_nop 0
	v_add_f32_e32 v17, 1.0, v17
	v_rcp_f32_e32 v23, v17
	s_nop 0
	v_pk_mul_f32 v[20:21], v[28:29], v[22:23]
	s_nop 0
	v_pk_mul_f32 v[18:19], v[18:19], v[20:21]
	v_lshlrev_b32_e32 v20, 16, v30
	v_and_b32_e32 v21, 0xffff0000, v30
	v_med3_f32 v20, v20, s70, v190
	v_med3_f32 v21, v21, s70, v190
	v_mov_b32_e32 v22, v33
	v_cvt_pk_fp8_f32 v22, v20, v21
	v_cvt_pk_bf16_f32 v17, v18, v19
	v_lshlrev_b32_e32 v18, 16, v24
	v_and_b32_e32 v19, 0xffff0000, v24
	v_med3_f32 v18, v18, s70, v190
	v_med3_f32 v19, v19, s70, v190
	v_cvt_pk_fp8_f32 v22, v18, v19 op_sel:[0,0,1]
	v_lshlrev_b32_e32 v18, 16, v16
	v_and_b32_e32 v16, 0xffff0000, v16
	v_med3_f32 v18, v18, s70, v190
	v_med3_f32 v16, v16, s70, v190
	v_mov_b32_e32 v23, v33
	v_cvt_pk_fp8_f32 v23, v18, v16
	v_lshlrev_b32_e32 v19, 16, v17
	v_and_b32_e32 v17, 0xffff0000, v17
	v_med3_f32 v16, v19, s70, v190
	v_med3_f32 v17, v17, s70, v190
	v_cvt_pk_fp8_f32 v23, v16, v17 op_sel:[0,0,1]
	global_store_dwordx2 v[110:111], v[22:23], off offset:2048
	s_cbranch_scc1 .LBB0_484
